# EpiRes bf16-residual epilogues P4/P9: all 16 residual loads hoisted to epilogue top, counted vmcnt(15)
# baseline (speedup 1.0000x reference)
.LBB0_574:
	v_mbcnt_lo_u32_b32 v132, -1, 0
	v_mbcnt_hi_u32_b32 v132, -1, v132
	global_load_dword v136, v148, s[8:9]
	s_lshl_b32 s24, s60, 8
	v_ashrrev_i32_e32 v133, 1, v132
	s_or_b32 s24, s24, s47
	v_and_b32_e32 v133, -8, v133
	v_add_u32_e32 v140, s24, v133
	s_lshl_b32 s24, s59, 8
	s_add_i32 s24, s24, s46
	v_and_or_b32 v142, v132, 15, s24
	v_ashrrev_i32_e32 v143, 31, v142
	v_ashrrev_i32_e32 v141, 31, v140
	v_lshlrev_b64 v[132:133], 11, v[142:143]
	v_lshl_add_u64 v[132:133], v[132:133], 0, v[140:141]
	v_lshlrev_b64 v[138:139], 1, v[132:133]
	v_lshl_add_u64 v[150:151], s[76:77], 0, v[138:139]
	global_load_dwordx4 v[132:135], v[150:151], off
	global_load_dwordx4 v[164:167], v[150:151], off offset:256
	s_mov_b64 s[98:99], 0x10000
	v_lshl_add_u64 v[224:225], v[150:151], 0, s[98:99]
	global_load_dwordx4 v[168:171], v[224:225], off
	global_load_dwordx4 v[172:175], v[224:225], off offset:256
	v_lshl_add_u64 v[224:225], v[224:225], 0, s[98:99]
	global_load_dwordx4 v[176:179], v[224:225], off
	global_load_dwordx4 v[180:183], v[224:225], off offset:256
	v_lshl_add_u64 v[224:225], v[224:225], 0, s[98:99]
	global_load_dwordx4 v[184:187], v[224:225], off
	global_load_dwordx4 v[188:191], v[224:225], off offset:256
	v_lshl_add_u64 v[224:225], v[150:151], 0, s[14:15]
	global_load_dwordx4 v[192:195], v[224:225], off
	global_load_dwordx4 v[196:199], v[224:225], off offset:256
	v_lshl_add_u64 v[224:225], v[150:151], 0, s[16:17]
	global_load_dwordx4 v[200:203], v[224:225], off
	global_load_dwordx4 v[204:207], v[224:225], off offset:256
	v_lshl_add_u64 v[224:225], v[150:151], 0, s[18:19]
	global_load_dwordx4 v[208:211], v[224:225], off
	global_load_dwordx4 v[212:215], v[224:225], off offset:256
	v_lshl_add_u64 v[224:225], v[150:151], 0, s[6:7]
	global_load_dwordx4 v[216:219], v[224:225], off
	global_load_dwordx4 v[220:223], v[224:225], off offset:256
	v_lshl_add_u64 v[152:153], s[64:65], 0, v[138:139]
	s_waitcnt vmcnt(16)
	v_div_scale_f32 v143, s[24:25], v136, v136, 1.0
	v_rcp_f32_e32 v149, v143
	v_div_scale_f32 v158, vcc, 1.0, v136, 1.0
	v_fma_f32 v154, -v143, v149, 1.0
	v_fmac_f32_e32 v149, v154, v149
	v_mul_f32_e32 v159, v158, v149
	v_fma_f32 v160, -v143, v159, v158
	v_fmac_f32_e32 v159, v160, v149
	v_fma_f32 v143, -v143, v159, v158
	v_div_fmas_f32 v143, v143, v149, v159
	v_div_fixup_f32 v136, v143, v136, 1.0
	s_andn2_b64 vcc, exec, s[0:1]
	s_waitcnt vmcnt(15)
	v_lshlrev_b32_e32 v154, 16, v132
	v_and_b32_e32 v155, 0xffff0000, v132
	v_lshlrev_b32_e32 v132, 16, v133
	v_and_b32_e32 v133, 0xffff0000, v133
	v_lshlrev_b32_e32 v156, 16, v134
	v_and_b32_e32 v157, 0xffff0000, v134
	v_lshlrev_b32_e32 v134, 16, v135
	v_and_b32_e32 v135, 0xffff0000, v135
	v_pk_mul_f32 v[132:133], v[132:133], s[12:13] op_sel_hi:[1,0]
	v_pk_mul_f32 v[156:157], v[156:157], s[12:13] op_sel_hi:[1,0]
	v_pk_mul_f32 v[134:135], v[134:135], s[12:13] op_sel_hi:[1,0]
	v_pk_mul_f32 v[154:155], v[154:155], s[12:13] op_sel_hi:[1,0]
	v_pk_fma_f32 v[126:127], v[126:127], v[136:137], v[132:133] op_sel_hi:[1,0,1]
	v_pk_fma_f32 v[132:133], v[122:123], v[136:137], v[134:135] op_sel_hi:[1,0,1]
	v_pk_fma_f32 v[122:123], v[120:121], v[136:137], v[156:157] op_sel_hi:[1,0,1]
	v_pk_fma_f32 v[124:125], v[124:125], v[136:137], v[154:155] op_sel_hi:[1,0,1]
	s_mov_b64 s[0:1], -1
	v_cvt_pk_bf16_f32 v120, v124, v125
	v_cvt_pk_bf16_f32 v121, v126, v127
	v_cvt_pk_bf16_f32 v122, v122, v123
	v_cvt_pk_bf16_f32 v123, v132, v133
	global_store_dwordx4 v[152:153], v[120:123], off
	v_or_b32_e32 v124, 16, v142
	v_ashrrev_i32_e32 v125, 31, v124
	v_lshlrev_b64 v[124:125], 11, v[124:125]
	v_lshl_add_u64 v[124:125], v[124:125], 0, v[140:141]
	v_lshlrev_b64 v[124:125], 1, v[124:125]
	s_waitcnt vmcnt(15)
	v_lshlrev_b32_e32 v132, 16, v164
	v_and_b32_e32 v133, 0xffff0000, v164
	v_lshlrev_b32_e32 v120, 16, v165
	v_and_b32_e32 v121, 0xffff0000, v165
	v_lshlrev_b32_e32 v134, 16, v166
	v_and_b32_e32 v135, 0xffff0000, v166
	v_lshlrev_b32_e32 v122, 16, v167
	v_and_b32_e32 v123, 0xffff0000, v167
	v_pk_mul_f32 v[120:121], v[120:121], s[12:13] op_sel_hi:[1,0]
	v_pk_mul_f32 v[134:135], v[134:135], s[12:13] op_sel_hi:[1,0]
	v_pk_mul_f32 v[122:123], v[122:123], s[12:13] op_sel_hi:[1,0]
	v_pk_mul_f32 v[132:133], v[132:133], s[12:13] op_sel_hi:[1,0]
	v_pk_fma_f32 v[118:119], v[118:119], v[136:137], v[120:121] op_sel_hi:[1,0,1]
	v_pk_fma_f32 v[120:121], v[114:115], v[136:137], v[122:123] op_sel_hi:[1,0,1]
	v_pk_fma_f32 v[114:115], v[112:113], v[136:137], v[134:135] op_sel_hi:[1,0,1]
	v_pk_fma_f32 v[116:117], v[116:117], v[136:137], v[132:133] op_sel_hi:[1,0,1]
	s_nop 0
	v_cvt_pk_bf16_f32 v112, v116, v117
	v_cvt_pk_bf16_f32 v113, v118, v119
	v_cvt_pk_bf16_f32 v114, v114, v115
	v_cvt_pk_bf16_f32 v115, v120, v121
	global_store_dwordx4 v[152:153], v[112:115], off offset:256
	v_lshl_add_u64 v[116:117], s[64:65], 0, v[124:125]
	s_waitcnt vmcnt(15)
	v_lshlrev_b32_e32 v118, 16, v168
	v_and_b32_e32 v119, 0xffff0000, v168
	v_lshlrev_b32_e32 v112, 16, v169
	v_and_b32_e32 v113, 0xffff0000, v169
	v_lshlrev_b32_e32 v120, 16, v170
	v_and_b32_e32 v121, 0xffff0000, v170
	v_lshlrev_b32_e32 v114, 16, v171
	v_and_b32_e32 v115, 0xffff0000, v171
	v_pk_mul_f32 v[112:113], v[112:113], s[12:13] op_sel_hi:[1,0]
	v_pk_mul_f32 v[120:121], v[120:121], s[12:13] op_sel_hi:[1,0]
	v_pk_mul_f32 v[114:115], v[114:115], s[12:13] op_sel_hi:[1,0]
	v_pk_mul_f32 v[118:119], v[118:119], s[12:13] op_sel_hi:[1,0]
	v_pk_fma_f32 v[110:111], v[110:111], v[136:137], v[112:113] op_sel_hi:[1,0,1]
	v_pk_fma_f32 v[112:113], v[106:107], v[136:137], v[114:115] op_sel_hi:[1,0,1]
	v_pk_fma_f32 v[106:107], v[104:105], v[136:137], v[120:121] op_sel_hi:[1,0,1]
	v_pk_fma_f32 v[108:109], v[108:109], v[136:137], v[118:119] op_sel_hi:[1,0,1]
	s_nop 0
	v_cvt_pk_bf16_f32 v104, v108, v109
	v_cvt_pk_bf16_f32 v105, v110, v111
	v_cvt_pk_bf16_f32 v106, v106, v107
	v_cvt_pk_bf16_f32 v107, v112, v113
	global_store_dwordx4 v[116:117], v[104:107], off
	v_or_b32_e32 v108, 32, v142
	v_ashrrev_i32_e32 v109, 31, v108
	v_lshlrev_b64 v[108:109], 11, v[108:109]
	v_lshl_add_u64 v[108:109], v[108:109], 0, v[140:141]
	v_lshlrev_b64 v[108:109], 1, v[108:109]
	s_waitcnt vmcnt(15)
	v_lshlrev_b32_e32 v112, 16, v172
	v_and_b32_e32 v113, 0xffff0000, v172
	v_lshlrev_b32_e32 v104, 16, v173
	v_and_b32_e32 v105, 0xffff0000, v173
	v_lshlrev_b32_e32 v114, 16, v174
	v_and_b32_e32 v115, 0xffff0000, v174
	v_lshlrev_b32_e32 v106, 16, v175
	v_and_b32_e32 v107, 0xffff0000, v175
	v_pk_mul_f32 v[104:105], v[104:105], s[12:13] op_sel_hi:[1,0]
	v_pk_mul_f32 v[114:115], v[114:115], s[12:13] op_sel_hi:[1,0]
	v_pk_mul_f32 v[106:107], v[106:107], s[12:13] op_sel_hi:[1,0]
	v_pk_mul_f32 v[112:113], v[112:113], s[12:13] op_sel_hi:[1,0]
	v_pk_fma_f32 v[102:103], v[102:103], v[136:137], v[104:105] op_sel_hi:[1,0,1]
	v_pk_fma_f32 v[104:105], v[98:99], v[136:137], v[106:107] op_sel_hi:[1,0,1]
	v_pk_fma_f32 v[98:99], v[96:97], v[136:137], v[114:115] op_sel_hi:[1,0,1]
	v_pk_fma_f32 v[100:101], v[100:101], v[136:137], v[112:113] op_sel_hi:[1,0,1]
	s_nop 0
	v_cvt_pk_bf16_f32 v96, v100, v101
	v_cvt_pk_bf16_f32 v97, v102, v103
	v_cvt_pk_bf16_f32 v98, v98, v99
	v_cvt_pk_bf16_f32 v99, v104, v105
	global_store_dwordx4 v[116:117], v[96:99], off offset:256
	v_lshl_add_u64 v[100:101], s[64:65], 0, v[108:109]
	s_waitcnt vmcnt(15)
	v_lshlrev_b32_e32 v102, 16, v176
	v_and_b32_e32 v103, 0xffff0000, v176
	v_lshlrev_b32_e32 v96, 16, v177
	v_and_b32_e32 v97, 0xffff0000, v177
	v_lshlrev_b32_e32 v104, 16, v178
	v_and_b32_e32 v105, 0xffff0000, v178
	v_lshlrev_b32_e32 v98, 16, v179
	v_and_b32_e32 v99, 0xffff0000, v179
	v_pk_mul_f32 v[96:97], v[96:97], s[12:13] op_sel_hi:[1,0]
	v_pk_mul_f32 v[104:105], v[104:105], s[12:13] op_sel_hi:[1,0]
	v_pk_mul_f32 v[98:99], v[98:99], s[12:13] op_sel_hi:[1,0]
	v_pk_mul_f32 v[102:103], v[102:103], s[12:13] op_sel_hi:[1,0]
	v_pk_fma_f32 v[94:95], v[94:95], v[136:137], v[96:97] op_sel_hi:[1,0,1]
	v_pk_fma_f32 v[96:97], v[90:91], v[136:137], v[98:99] op_sel_hi:[1,0,1]
	v_pk_fma_f32 v[90:91], v[88:89], v[136:137], v[104:105] op_sel_hi:[1,0,1]
	v_pk_fma_f32 v[92:93], v[92:93], v[136:137], v[102:103] op_sel_hi:[1,0,1]
	s_nop 0
	v_cvt_pk_bf16_f32 v88, v92, v93
	v_cvt_pk_bf16_f32 v89, v94, v95
	v_cvt_pk_bf16_f32 v90, v90, v91
	v_cvt_pk_bf16_f32 v91, v96, v97
	global_store_dwordx4 v[100:101], v[88:91], off
	v_or_b32_e32 v92, 48, v142
	v_ashrrev_i32_e32 v93, 31, v92
	v_lshlrev_b64 v[92:93], 11, v[92:93]
	v_lshl_add_u64 v[92:93], v[92:93], 0, v[140:141]
	v_lshlrev_b64 v[92:93], 1, v[92:93]
	s_waitcnt vmcnt(15)
	v_lshlrev_b32_e32 v96, 16, v180
	v_and_b32_e32 v97, 0xffff0000, v180
	v_lshlrev_b32_e32 v88, 16, v181
	v_and_b32_e32 v89, 0xffff0000, v181
	v_lshlrev_b32_e32 v98, 16, v182
	v_and_b32_e32 v99, 0xffff0000, v182
	v_lshlrev_b32_e32 v90, 16, v183
	v_and_b32_e32 v91, 0xffff0000, v183
	v_pk_mul_f32 v[88:89], v[88:89], s[12:13] op_sel_hi:[1,0]
	v_pk_mul_f32 v[98:99], v[98:99], s[12:13] op_sel_hi:[1,0]
	v_pk_mul_f32 v[90:91], v[90:91], s[12:13] op_sel_hi:[1,0]
	v_pk_mul_f32 v[96:97], v[96:97], s[12:13] op_sel_hi:[1,0]
	v_pk_fma_f32 v[86:87], v[86:87], v[136:137], v[88:89] op_sel_hi:[1,0,1]
	v_pk_fma_f32 v[88:89], v[82:83], v[136:137], v[90:91] op_sel_hi:[1,0,1]
	v_pk_fma_f32 v[82:83], v[80:81], v[136:137], v[98:99] op_sel_hi:[1,0,1]
	v_pk_fma_f32 v[84:85], v[84:85], v[136:137], v[96:97] op_sel_hi:[1,0,1]
	s_nop 0
	v_cvt_pk_bf16_f32 v80, v84, v85
	v_cvt_pk_bf16_f32 v81, v86, v87
	v_cvt_pk_bf16_f32 v82, v82, v83
	v_cvt_pk_bf16_f32 v83, v88, v89
	global_store_dwordx4 v[100:101], v[80:83], off offset:256
	v_lshl_add_u64 v[84:85], s[64:65], 0, v[92:93]
	s_waitcnt vmcnt(15)
	v_lshlrev_b32_e32 v86, 16, v184
	v_and_b32_e32 v87, 0xffff0000, v184
	v_lshlrev_b32_e32 v80, 16, v185
	v_and_b32_e32 v81, 0xffff0000, v185
	v_lshlrev_b32_e32 v88, 16, v186
	v_and_b32_e32 v89, 0xffff0000, v186
	v_lshlrev_b32_e32 v82, 16, v187
	v_and_b32_e32 v83, 0xffff0000, v187
	v_pk_mul_f32 v[80:81], v[80:81], s[12:13] op_sel_hi:[1,0]
	v_pk_mul_f32 v[88:89], v[88:89], s[12:13] op_sel_hi:[1,0]
	v_pk_mul_f32 v[82:83], v[82:83], s[12:13] op_sel_hi:[1,0]
	v_pk_mul_f32 v[86:87], v[86:87], s[12:13] op_sel_hi:[1,0]
	v_pk_fma_f32 v[78:79], v[78:79], v[136:137], v[80:81] op_sel_hi:[1,0,1]
	v_pk_fma_f32 v[80:81], v[74:75], v[136:137], v[82:83] op_sel_hi:[1,0,1]
	v_pk_fma_f32 v[74:75], v[72:73], v[136:137], v[88:89] op_sel_hi:[1,0,1]
	v_pk_fma_f32 v[76:77], v[76:77], v[136:137], v[86:87] op_sel_hi:[1,0,1]
	s_nop 0
	v_cvt_pk_bf16_f32 v72, v76, v77
	v_cvt_pk_bf16_f32 v73, v78, v79
	v_cvt_pk_bf16_f32 v74, v74, v75
	v_cvt_pk_bf16_f32 v75, v80, v81
	global_store_dwordx4 v[84:85], v[72:75], off
	v_lshl_add_u64 v[76:77], v[138:139], 0, s[14:15]
	s_waitcnt vmcnt(15)
	v_lshlrev_b32_e32 v80, 16, v188
	v_and_b32_e32 v81, 0xffff0000, v188
	v_lshlrev_b32_e32 v72, 16, v189
	v_and_b32_e32 v73, 0xffff0000, v189
	v_lshlrev_b32_e32 v82, 16, v190
	v_and_b32_e32 v83, 0xffff0000, v190
	v_lshlrev_b32_e32 v74, 16, v191
	v_and_b32_e32 v75, 0xffff0000, v191
	v_pk_mul_f32 v[72:73], v[72:73], s[12:13] op_sel_hi:[1,0]
	v_pk_mul_f32 v[82:83], v[82:83], s[12:13] op_sel_hi:[1,0]
	v_pk_mul_f32 v[74:75], v[74:75], s[12:13] op_sel_hi:[1,0]
	v_pk_mul_f32 v[80:81], v[80:81], s[12:13] op_sel_hi:[1,0]
	v_pk_fma_f32 v[70:71], v[70:71], v[136:137], v[72:73] op_sel_hi:[1,0,1]
	v_pk_fma_f32 v[72:73], v[66:67], v[136:137], v[74:75] op_sel_hi:[1,0,1]
	v_pk_fma_f32 v[66:67], v[64:65], v[136:137], v[82:83] op_sel_hi:[1,0,1]
	v_pk_fma_f32 v[68:69], v[68:69], v[136:137], v[80:81] op_sel_hi:[1,0,1]
	s_nop 0
	v_cvt_pk_bf16_f32 v64, v68, v69
	v_cvt_pk_bf16_f32 v65, v70, v71
	v_cvt_pk_bf16_f32 v66, v66, v67
	v_cvt_pk_bf16_f32 v67, v72, v73
	global_store_dwordx4 v[84:85], v[64:67], off offset:256
	v_lshl_add_u64 v[68:69], s[64:65], 0, v[76:77]
	s_waitcnt vmcnt(15)
	v_lshlrev_b32_e32 v70, 16, v192
	v_and_b32_e32 v71, 0xffff0000, v192
	v_lshlrev_b32_e32 v64, 16, v193
	v_and_b32_e32 v65, 0xffff0000, v193
	v_lshlrev_b32_e32 v72, 16, v194
	v_and_b32_e32 v73, 0xffff0000, v194
	v_lshlrev_b32_e32 v66, 16, v195
	v_and_b32_e32 v67, 0xffff0000, v195
	v_pk_mul_f32 v[64:65], v[64:65], s[12:13] op_sel_hi:[1,0]
	v_pk_mul_f32 v[72:73], v[72:73], s[12:13] op_sel_hi:[1,0]
	v_pk_mul_f32 v[66:67], v[66:67], s[12:13] op_sel_hi:[1,0]
	v_pk_mul_f32 v[70:71], v[70:71], s[12:13] op_sel_hi:[1,0]
	v_pk_fma_f32 v[62:63], v[62:63], v[136:137], v[64:65] op_sel_hi:[1,0,1]
	v_pk_fma_f32 v[64:65], v[58:59], v[136:137], v[66:67] op_sel_hi:[1,0,1]
	v_pk_fma_f32 v[58:59], v[56:57], v[136:137], v[72:73] op_sel_hi:[1,0,1]
	v_pk_fma_f32 v[60:61], v[60:61], v[136:137], v[70:71] op_sel_hi:[1,0,1]
	s_nop 0
	v_cvt_pk_bf16_f32 v56, v60, v61
	v_cvt_pk_bf16_f32 v57, v62, v63
	v_cvt_pk_bf16_f32 v58, v58, v59
	v_cvt_pk_bf16_f32 v59, v64, v65
	global_store_dwordx4 v[68:69], v[56:59], off
	v_lshl_add_u64 v[60:61], v[138:139], 0, s[16:17]
	s_waitcnt vmcnt(15)
	v_lshlrev_b32_e32 v64, 16, v196
	v_and_b32_e32 v65, 0xffff0000, v196
	v_lshlrev_b32_e32 v56, 16, v197
	v_and_b32_e32 v57, 0xffff0000, v197
	v_lshlrev_b32_e32 v66, 16, v198
	v_and_b32_e32 v67, 0xffff0000, v198
	v_lshlrev_b32_e32 v58, 16, v199
	v_and_b32_e32 v59, 0xffff0000, v199
	v_pk_mul_f32 v[56:57], v[56:57], s[12:13] op_sel_hi:[1,0]
	v_pk_mul_f32 v[66:67], v[66:67], s[12:13] op_sel_hi:[1,0]
	v_pk_mul_f32 v[58:59], v[58:59], s[12:13] op_sel_hi:[1,0]
	v_pk_mul_f32 v[64:65], v[64:65], s[12:13] op_sel_hi:[1,0]
	v_pk_fma_f32 v[54:55], v[54:55], v[136:137], v[56:57] op_sel_hi:[1,0,1]
	v_pk_fma_f32 v[56:57], v[50:51], v[136:137], v[58:59] op_sel_hi:[1,0,1]
	v_pk_fma_f32 v[50:51], v[48:49], v[136:137], v[66:67] op_sel_hi:[1,0,1]
	v_pk_fma_f32 v[52:53], v[52:53], v[136:137], v[64:65] op_sel_hi:[1,0,1]
	s_nop 0
	v_cvt_pk_bf16_f32 v48, v52, v53
	v_cvt_pk_bf16_f32 v49, v54, v55
	v_cvt_pk_bf16_f32 v50, v50, v51
	v_cvt_pk_bf16_f32 v51, v56, v57
	global_store_dwordx4 v[68:69], v[48:51], off offset:256
	v_lshl_add_u64 v[52:53], s[64:65], 0, v[60:61]
	s_waitcnt vmcnt(15)
	v_lshlrev_b32_e32 v54, 16, v200
	v_and_b32_e32 v55, 0xffff0000, v200
	v_lshlrev_b32_e32 v48, 16, v201
	v_and_b32_e32 v49, 0xffff0000, v201
	v_lshlrev_b32_e32 v56, 16, v202
	v_and_b32_e32 v57, 0xffff0000, v202
	v_lshlrev_b32_e32 v50, 16, v203
	v_and_b32_e32 v51, 0xffff0000, v203
	v_pk_mul_f32 v[48:49], v[48:49], s[12:13] op_sel_hi:[1,0]
	v_pk_mul_f32 v[56:57], v[56:57], s[12:13] op_sel_hi:[1,0]
	v_pk_mul_f32 v[50:51], v[50:51], s[12:13] op_sel_hi:[1,0]
	v_pk_mul_f32 v[54:55], v[54:55], s[12:13] op_sel_hi:[1,0]
	v_pk_fma_f32 v[46:47], v[46:47], v[136:137], v[48:49] op_sel_hi:[1,0,1]
	v_pk_fma_f32 v[48:49], v[42:43], v[136:137], v[50:51] op_sel_hi:[1,0,1]
	v_pk_fma_f32 v[42:43], v[40:41], v[136:137], v[56:57] op_sel_hi:[1,0,1]
	v_pk_fma_f32 v[44:45], v[44:45], v[136:137], v[54:55] op_sel_hi:[1,0,1]
	s_nop 0
	v_cvt_pk_bf16_f32 v40, v44, v45
	v_cvt_pk_bf16_f32 v41, v46, v47
	v_cvt_pk_bf16_f32 v42, v42, v43
	v_cvt_pk_bf16_f32 v43, v48, v49
	global_store_dwordx4 v[52:53], v[40:43], off
	v_lshl_add_u64 v[44:45], v[138:139], 0, s[18:19]
	s_waitcnt vmcnt(15)
	v_lshlrev_b32_e32 v48, 16, v204
	v_and_b32_e32 v49, 0xffff0000, v204
	v_lshlrev_b32_e32 v40, 16, v205
	v_and_b32_e32 v41, 0xffff0000, v205
	v_lshlrev_b32_e32 v50, 16, v206
	v_and_b32_e32 v51, 0xffff0000, v206
	v_lshlrev_b32_e32 v42, 16, v207
	v_and_b32_e32 v43, 0xffff0000, v207
	v_pk_mul_f32 v[40:41], v[40:41], s[12:13] op_sel_hi:[1,0]
	v_pk_mul_f32 v[50:51], v[50:51], s[12:13] op_sel_hi:[1,0]
	v_pk_mul_f32 v[42:43], v[42:43], s[12:13] op_sel_hi:[1,0]
	v_pk_mul_f32 v[48:49], v[48:49], s[12:13] op_sel_hi:[1,0]
	v_pk_fma_f32 v[38:39], v[38:39], v[136:137], v[40:41] op_sel_hi:[1,0,1]
	v_pk_fma_f32 v[40:41], v[34:35], v[136:137], v[42:43] op_sel_hi:[1,0,1]
	v_pk_fma_f32 v[34:35], v[32:33], v[136:137], v[50:51] op_sel_hi:[1,0,1]
	v_pk_fma_f32 v[36:37], v[36:37], v[136:137], v[48:49] op_sel_hi:[1,0,1]
	s_nop 0
	v_cvt_pk_bf16_f32 v32, v36, v37
	v_cvt_pk_bf16_f32 v33, v38, v39
	v_cvt_pk_bf16_f32 v34, v34, v35
	v_cvt_pk_bf16_f32 v35, v40, v41
	global_store_dwordx4 v[52:53], v[32:35], off offset:256
	v_lshl_add_u64 v[36:37], s[64:65], 0, v[44:45]
	s_waitcnt vmcnt(15)
	v_lshlrev_b32_e32 v38, 16, v208
	v_and_b32_e32 v39, 0xffff0000, v208
	v_lshlrev_b32_e32 v32, 16, v209
	v_and_b32_e32 v33, 0xffff0000, v209
	v_lshlrev_b32_e32 v40, 16, v210
	v_and_b32_e32 v41, 0xffff0000, v210
	v_lshlrev_b32_e32 v34, 16, v211
	v_and_b32_e32 v35, 0xffff0000, v211
	v_pk_mul_f32 v[32:33], v[32:33], s[12:13] op_sel_hi:[1,0]
	v_pk_mul_f32 v[40:41], v[40:41], s[12:13] op_sel_hi:[1,0]
	v_pk_mul_f32 v[34:35], v[34:35], s[12:13] op_sel_hi:[1,0]
	v_pk_mul_f32 v[38:39], v[38:39], s[12:13] op_sel_hi:[1,0]
	v_pk_fma_f32 v[30:31], v[30:31], v[136:137], v[32:33] op_sel_hi:[1,0,1]
	v_pk_fma_f32 v[32:33], v[26:27], v[136:137], v[34:35] op_sel_hi:[1,0,1]
	v_pk_fma_f32 v[26:27], v[24:25], v[136:137], v[40:41] op_sel_hi:[1,0,1]
	v_pk_fma_f32 v[28:29], v[28:29], v[136:137], v[38:39] op_sel_hi:[1,0,1]
	s_nop 0
	v_cvt_pk_bf16_f32 v24, v28, v29
	v_cvt_pk_bf16_f32 v25, v30, v31
	v_cvt_pk_bf16_f32 v26, v26, v27
	v_cvt_pk_bf16_f32 v27, v32, v33
	global_store_dwordx4 v[36:37], v[24:27], off
	v_lshl_add_u64 v[28:29], v[138:139], 0, s[6:7]
	s_waitcnt vmcnt(15)
	v_lshlrev_b32_e32 v32, 16, v212
	v_and_b32_e32 v33, 0xffff0000, v212
	v_lshlrev_b32_e32 v24, 16, v213
	v_and_b32_e32 v25, 0xffff0000, v213
	v_lshlrev_b32_e32 v34, 16, v214
	v_and_b32_e32 v35, 0xffff0000, v214
	v_lshlrev_b32_e32 v26, 16, v215
	v_and_b32_e32 v27, 0xffff0000, v215
	v_pk_mul_f32 v[24:25], v[24:25], s[12:13] op_sel_hi:[1,0]
	v_pk_mul_f32 v[34:35], v[34:35], s[12:13] op_sel_hi:[1,0]
	v_pk_mul_f32 v[26:27], v[26:27], s[12:13] op_sel_hi:[1,0]
	v_pk_mul_f32 v[32:33], v[32:33], s[12:13] op_sel_hi:[1,0]
	v_pk_fma_f32 v[22:23], v[22:23], v[136:137], v[24:25] op_sel_hi:[1,0,1]
	v_pk_fma_f32 v[24:25], v[18:19], v[136:137], v[26:27] op_sel_hi:[1,0,1]
	v_pk_fma_f32 v[18:19], v[16:17], v[136:137], v[34:35] op_sel_hi:[1,0,1]
	v_pk_fma_f32 v[20:21], v[20:21], v[136:137], v[32:33] op_sel_hi:[1,0,1]
	s_nop 0
	v_cvt_pk_bf16_f32 v16, v20, v21
	v_cvt_pk_bf16_f32 v17, v22, v23
	v_cvt_pk_bf16_f32 v18, v18, v19
	v_cvt_pk_bf16_f32 v19, v24, v25
	global_store_dwordx4 v[36:37], v[16:19], off offset:256
	v_lshl_add_u64 v[20:21], s[64:65], 0, v[28:29]
	s_waitcnt vmcnt(15)
	v_lshlrev_b32_e32 v22, 16, v216
	v_and_b32_e32 v23, 0xffff0000, v216
	v_lshlrev_b32_e32 v16, 16, v217
	v_and_b32_e32 v17, 0xffff0000, v217
	v_lshlrev_b32_e32 v24, 16, v218
	v_and_b32_e32 v25, 0xffff0000, v218
	v_lshlrev_b32_e32 v18, 16, v219
	v_and_b32_e32 v19, 0xffff0000, v219
	v_pk_mul_f32 v[16:17], v[16:17], s[12:13] op_sel_hi:[1,0]
	v_pk_mul_f32 v[24:25], v[24:25], s[12:13] op_sel_hi:[1,0]
	v_pk_mul_f32 v[18:19], v[18:19], s[12:13] op_sel_hi:[1,0]
	v_pk_mul_f32 v[22:23], v[22:23], s[12:13] op_sel_hi:[1,0]
	v_pk_fma_f32 v[14:15], v[14:15], v[136:137], v[16:17] op_sel_hi:[1,0,1]
	v_pk_fma_f32 v[16:17], v[10:11], v[136:137], v[18:19] op_sel_hi:[1,0,1]
	v_pk_fma_f32 v[10:11], v[8:9], v[136:137], v[24:25] op_sel_hi:[1,0,1]
	v_pk_fma_f32 v[12:13], v[12:13], v[136:137], v[22:23] op_sel_hi:[1,0,1]
	s_nop 0
	v_cvt_pk_bf16_f32 v8, v12, v13
	v_cvt_pk_bf16_f32 v9, v14, v15
	v_cvt_pk_bf16_f32 v10, v10, v11
	v_cvt_pk_bf16_f32 v11, v16, v17
	global_store_dwordx4 v[20:21], v[8:11], off
	s_waitcnt vmcnt(15)
	v_lshlrev_b32_e32 v12, 16, v220
	v_and_b32_e32 v13, 0xffff0000, v220
	v_lshlrev_b32_e32 v8, 16, v221
	v_and_b32_e32 v9, 0xffff0000, v221
	v_lshlrev_b32_e32 v14, 16, v222
	v_and_b32_e32 v15, 0xffff0000, v222
	v_lshlrev_b32_e32 v10, 16, v223
	v_and_b32_e32 v11, 0xffff0000, v223
	v_pk_mul_f32 v[8:9], v[8:9], s[12:13] op_sel_hi:[1,0]
	v_pk_mul_f32 v[14:15], v[14:15], s[12:13] op_sel_hi:[1,0]
	v_pk_mul_f32 v[10:11], v[10:11], s[12:13] op_sel_hi:[1,0]
	v_pk_mul_f32 v[12:13], v[12:13], s[12:13] op_sel_hi:[1,0]
	v_pk_fma_f32 v[6:7], v[6:7], v[136:137], v[8:9] op_sel_hi:[1,0,1]
	v_pk_fma_f32 v[8:9], v[2:3], v[136:137], v[10:11] op_sel_hi:[1,0,1]
	v_pk_fma_f32 v[2:3], v[0:1], v[136:137], v[14:15] op_sel_hi:[1,0,1]
	v_pk_fma_f32 v[4:5], v[4:5], v[136:137], v[12:13] op_sel_hi:[1,0,1]
	s_nop 0
	v_cvt_pk_bf16_f32 v0, v4, v5
	v_cvt_pk_bf16_f32 v1, v6, v7
	v_cvt_pk_bf16_f32 v2, v2, v3
	v_cvt_pk_bf16_f32 v3, v8, v9
	global_store_dwordx4 v[20:21], v[0:3], off offset:256
	s_cbranch_vccnz .LBB0_563
	s_andn2_b64 vcc, exec, s[4:5]
	s_cbranch_vccnz .LBB0_562
	s_barrier
	s_branch .LBB0_562

.LBB0_1625:
	v_mbcnt_lo_u32_b32 v128, -1, 0
	v_mbcnt_hi_u32_b32 v128, -1, v128
	global_load_dword v132, v148, s[6:7]
	s_lshl_b32 s21, s30, 8
	v_ashrrev_i32_e32 v129, 1, v128
	s_or_b32 s21, s21, s53
	v_and_b32_e32 v129, -8, v129
	v_add_u32_e32 v136, s21, v129
	s_lshl_b32 s21, s28, 8
	s_add_i32 s21, s21, s52
	v_and_or_b32 v138, v128, 15, s21
	v_ashrrev_i32_e32 v139, 31, v138
	v_ashrrev_i32_e32 v137, 31, v136
	v_lshlrev_b64 v[128:129], 11, v[138:139]
	v_lshl_add_u64 v[128:129], v[128:129], 0, v[136:137]
	v_lshlrev_b64 v[134:135], 1, v[128:129]
	v_lshl_add_u64 v[150:151], s[76:77], 0, v[134:135]
	global_load_dwordx4 v[128:131], v[150:151], off
	global_load_dwordx4 v[164:167], v[150:151], off offset:256
	s_mov_b64 s[98:99], 0x10000
	v_lshl_add_u64 v[224:225], v[150:151], 0, s[98:99]
	global_load_dwordx4 v[168:171], v[224:225], off
	global_load_dwordx4 v[172:175], v[224:225], off offset:256
	v_lshl_add_u64 v[224:225], v[224:225], 0, s[98:99]
	global_load_dwordx4 v[176:179], v[224:225], off
	global_load_dwordx4 v[180:183], v[224:225], off offset:256
	v_lshl_add_u64 v[224:225], v[224:225], 0, s[98:99]
	global_load_dwordx4 v[184:187], v[224:225], off
	global_load_dwordx4 v[188:191], v[224:225], off offset:256
	v_lshl_add_u64 v[224:225], v[150:151], 0, s[12:13]
	global_load_dwordx4 v[192:195], v[224:225], off
	global_load_dwordx4 v[196:199], v[224:225], off offset:256
	v_lshl_add_u64 v[224:225], v[150:151], 0, s[14:15]
	global_load_dwordx4 v[200:203], v[224:225], off
	global_load_dwordx4 v[204:207], v[224:225], off offset:256
	v_lshl_add_u64 v[224:225], v[150:151], 0, s[16:17]
	global_load_dwordx4 v[208:211], v[224:225], off
	global_load_dwordx4 v[212:215], v[224:225], off offset:256
	v_lshl_add_u64 v[224:225], v[150:151], 0, s[18:19]
	global_load_dwordx4 v[216:219], v[224:225], off
	global_load_dwordx4 v[220:223], v[224:225], off offset:256
	v_lshl_add_u64 v[152:153], s[64:65], 0, v[134:135]
	s_waitcnt vmcnt(16)
	v_div_scale_f32 v139, s[34:35], v132, v132, 1.0
	v_rcp_f32_e32 v149, v139
	v_div_scale_f32 v158, vcc, 1.0, v132, 1.0
	v_fma_f32 v154, -v139, v149, 1.0
	v_fmac_f32_e32 v149, v154, v149
	v_mul_f32_e32 v159, v158, v149
	v_fma_f32 v160, -v139, v159, v158
	v_fmac_f32_e32 v159, v160, v149
	v_fma_f32 v139, -v139, v159, v158
	v_div_fmas_f32 v139, v139, v149, v159
	v_div_fixup_f32 v132, v139, v132, 1.0
	s_andn2_b64 vcc, exec, s[0:1]
	s_waitcnt vmcnt(15)
	v_lshlrev_b32_e32 v154, 16, v128
	v_and_b32_e32 v155, 0xffff0000, v128
	v_lshlrev_b32_e32 v128, 16, v129
	v_and_b32_e32 v129, 0xffff0000, v129
	v_lshlrev_b32_e32 v156, 16, v130
	v_and_b32_e32 v157, 0xffff0000, v130
	v_lshlrev_b32_e32 v130, 16, v131
	v_and_b32_e32 v131, 0xffff0000, v131
	v_pk_mul_f32 v[128:129], v[128:129], s[10:11] op_sel_hi:[1,0]
	v_pk_mul_f32 v[156:157], v[156:157], s[10:11] op_sel_hi:[1,0]
	v_pk_mul_f32 v[130:131], v[130:131], s[10:11] op_sel_hi:[1,0]
	v_pk_mul_f32 v[154:155], v[154:155], s[10:11] op_sel_hi:[1,0]
	v_pk_fma_f32 v[126:127], v[126:127], v[132:133], v[128:129] op_sel_hi:[1,0,1]
	v_pk_fma_f32 v[128:129], v[122:123], v[132:133], v[130:131] op_sel_hi:[1,0,1]
	v_pk_fma_f32 v[122:123], v[120:121], v[132:133], v[156:157] op_sel_hi:[1,0,1]
	v_pk_fma_f32 v[124:125], v[124:125], v[132:133], v[154:155] op_sel_hi:[1,0,1]
	s_mov_b64 s[0:1], -1
	v_cvt_pk_bf16_f32 v120, v124, v125
	v_cvt_pk_bf16_f32 v121, v126, v127
	v_cvt_pk_bf16_f32 v122, v122, v123
	v_cvt_pk_bf16_f32 v123, v128, v129
	global_store_dwordx4 v[152:153], v[120:123], off
	v_or_b32_e32 v124, 16, v138
	v_ashrrev_i32_e32 v125, 31, v124
	v_lshlrev_b64 v[124:125], 11, v[124:125]
	v_lshl_add_u64 v[124:125], v[124:125], 0, v[136:137]
	v_lshlrev_b64 v[124:125], 1, v[124:125]
	s_waitcnt vmcnt(15)
	v_lshlrev_b32_e32 v128, 16, v164
	v_and_b32_e32 v129, 0xffff0000, v164
	v_lshlrev_b32_e32 v120, 16, v165
	v_and_b32_e32 v121, 0xffff0000, v165
	v_lshlrev_b32_e32 v130, 16, v166
	v_and_b32_e32 v131, 0xffff0000, v166
	v_lshlrev_b32_e32 v122, 16, v167
	v_and_b32_e32 v123, 0xffff0000, v167
	v_pk_mul_f32 v[120:121], v[120:121], s[10:11] op_sel_hi:[1,0]
	v_pk_mul_f32 v[130:131], v[130:131], s[10:11] op_sel_hi:[1,0]
	v_pk_mul_f32 v[122:123], v[122:123], s[10:11] op_sel_hi:[1,0]
	v_pk_mul_f32 v[128:129], v[128:129], s[10:11] op_sel_hi:[1,0]
	v_pk_fma_f32 v[118:119], v[118:119], v[132:133], v[120:121] op_sel_hi:[1,0,1]
	v_pk_fma_f32 v[120:121], v[114:115], v[132:133], v[122:123] op_sel_hi:[1,0,1]
	v_pk_fma_f32 v[114:115], v[112:113], v[132:133], v[130:131] op_sel_hi:[1,0,1]
	v_pk_fma_f32 v[116:117], v[116:117], v[132:133], v[128:129] op_sel_hi:[1,0,1]
	s_nop 0
	v_cvt_pk_bf16_f32 v112, v116, v117
	v_cvt_pk_bf16_f32 v113, v118, v119
	v_cvt_pk_bf16_f32 v114, v114, v115
	v_cvt_pk_bf16_f32 v115, v120, v121
	global_store_dwordx4 v[152:153], v[112:115], off offset:256
	v_lshl_add_u64 v[116:117], s[64:65], 0, v[124:125]
	s_waitcnt vmcnt(15)
	v_lshlrev_b32_e32 v118, 16, v168
	v_and_b32_e32 v119, 0xffff0000, v168
	v_lshlrev_b32_e32 v112, 16, v169
	v_and_b32_e32 v113, 0xffff0000, v169
	v_lshlrev_b32_e32 v120, 16, v170
	v_and_b32_e32 v121, 0xffff0000, v170
	v_lshlrev_b32_e32 v114, 16, v171
	v_and_b32_e32 v115, 0xffff0000, v171
	v_pk_mul_f32 v[112:113], v[112:113], s[10:11] op_sel_hi:[1,0]
	v_pk_mul_f32 v[120:121], v[120:121], s[10:11] op_sel_hi:[1,0]
	v_pk_mul_f32 v[114:115], v[114:115], s[10:11] op_sel_hi:[1,0]
	v_pk_mul_f32 v[118:119], v[118:119], s[10:11] op_sel_hi:[1,0]
	v_pk_fma_f32 v[110:111], v[110:111], v[132:133], v[112:113] op_sel_hi:[1,0,1]
	v_pk_fma_f32 v[112:113], v[106:107], v[132:133], v[114:115] op_sel_hi:[1,0,1]
	v_pk_fma_f32 v[106:107], v[104:105], v[132:133], v[120:121] op_sel_hi:[1,0,1]
	v_pk_fma_f32 v[108:109], v[108:109], v[132:133], v[118:119] op_sel_hi:[1,0,1]
	s_nop 0
	v_cvt_pk_bf16_f32 v104, v108, v109
	v_cvt_pk_bf16_f32 v105, v110, v111
	v_cvt_pk_bf16_f32 v106, v106, v107
	v_cvt_pk_bf16_f32 v107, v112, v113
	global_store_dwordx4 v[116:117], v[104:107], off
	v_or_b32_e32 v108, 32, v138
	v_ashrrev_i32_e32 v109, 31, v108
	v_lshlrev_b64 v[108:109], 11, v[108:109]
	v_lshl_add_u64 v[108:109], v[108:109], 0, v[136:137]
	v_lshlrev_b64 v[108:109], 1, v[108:109]
	s_waitcnt vmcnt(15)
	v_lshlrev_b32_e32 v112, 16, v172
	v_and_b32_e32 v113, 0xffff0000, v172
	v_lshlrev_b32_e32 v104, 16, v173
	v_and_b32_e32 v105, 0xffff0000, v173
	v_lshlrev_b32_e32 v114, 16, v174
	v_and_b32_e32 v115, 0xffff0000, v174
	v_lshlrev_b32_e32 v106, 16, v175
	v_and_b32_e32 v107, 0xffff0000, v175
	v_pk_mul_f32 v[104:105], v[104:105], s[10:11] op_sel_hi:[1,0]
	v_pk_mul_f32 v[114:115], v[114:115], s[10:11] op_sel_hi:[1,0]
	v_pk_mul_f32 v[106:107], v[106:107], s[10:11] op_sel_hi:[1,0]
	v_pk_mul_f32 v[112:113], v[112:113], s[10:11] op_sel_hi:[1,0]
	v_pk_fma_f32 v[102:103], v[102:103], v[132:133], v[104:105] op_sel_hi:[1,0,1]
	v_pk_fma_f32 v[104:105], v[98:99], v[132:133], v[106:107] op_sel_hi:[1,0,1]
	v_pk_fma_f32 v[98:99], v[96:97], v[132:133], v[114:115] op_sel_hi:[1,0,1]
	v_pk_fma_f32 v[100:101], v[100:101], v[132:133], v[112:113] op_sel_hi:[1,0,1]
	s_nop 0
	v_cvt_pk_bf16_f32 v96, v100, v101
	v_cvt_pk_bf16_f32 v97, v102, v103
	v_cvt_pk_bf16_f32 v98, v98, v99
	v_cvt_pk_bf16_f32 v99, v104, v105
	global_store_dwordx4 v[116:117], v[96:99], off offset:256
	v_lshl_add_u64 v[100:101], s[64:65], 0, v[108:109]
	s_waitcnt vmcnt(15)
	v_lshlrev_b32_e32 v102, 16, v176
	v_and_b32_e32 v103, 0xffff0000, v176
	v_lshlrev_b32_e32 v96, 16, v177
	v_and_b32_e32 v97, 0xffff0000, v177
	v_lshlrev_b32_e32 v104, 16, v178
	v_and_b32_e32 v105, 0xffff0000, v178
	v_lshlrev_b32_e32 v98, 16, v179
	v_and_b32_e32 v99, 0xffff0000, v179
	v_pk_mul_f32 v[96:97], v[96:97], s[10:11] op_sel_hi:[1,0]
	v_pk_mul_f32 v[104:105], v[104:105], s[10:11] op_sel_hi:[1,0]
	v_pk_mul_f32 v[98:99], v[98:99], s[10:11] op_sel_hi:[1,0]
	v_pk_mul_f32 v[102:103], v[102:103], s[10:11] op_sel_hi:[1,0]
	v_pk_fma_f32 v[94:95], v[94:95], v[132:133], v[96:97] op_sel_hi:[1,0,1]
	v_pk_fma_f32 v[96:97], v[90:91], v[132:133], v[98:99] op_sel_hi:[1,0,1]
	v_pk_fma_f32 v[90:91], v[88:89], v[132:133], v[104:105] op_sel_hi:[1,0,1]
	v_pk_fma_f32 v[92:93], v[92:93], v[132:133], v[102:103] op_sel_hi:[1,0,1]
	s_nop 0
	v_cvt_pk_bf16_f32 v88, v92, v93
	v_cvt_pk_bf16_f32 v89, v94, v95
	v_cvt_pk_bf16_f32 v90, v90, v91
	v_cvt_pk_bf16_f32 v91, v96, v97
	global_store_dwordx4 v[100:101], v[88:91], off
	v_or_b32_e32 v92, 48, v138
	v_ashrrev_i32_e32 v93, 31, v92
	v_lshlrev_b64 v[92:93], 11, v[92:93]
	v_lshl_add_u64 v[92:93], v[92:93], 0, v[136:137]
	v_lshlrev_b64 v[92:93], 1, v[92:93]
	s_waitcnt vmcnt(15)
	v_lshlrev_b32_e32 v96, 16, v180
	v_and_b32_e32 v97, 0xffff0000, v180
	v_lshlrev_b32_e32 v88, 16, v181
	v_and_b32_e32 v89, 0xffff0000, v181
	v_lshlrev_b32_e32 v98, 16, v182
	v_and_b32_e32 v99, 0xffff0000, v182
	v_lshlrev_b32_e32 v90, 16, v183
	v_and_b32_e32 v91, 0xffff0000, v183
	v_pk_mul_f32 v[88:89], v[88:89], s[10:11] op_sel_hi:[1,0]
	v_pk_mul_f32 v[98:99], v[98:99], s[10:11] op_sel_hi:[1,0]
	v_pk_mul_f32 v[90:91], v[90:91], s[10:11] op_sel_hi:[1,0]
	v_pk_mul_f32 v[96:97], v[96:97], s[10:11] op_sel_hi:[1,0]
	v_pk_fma_f32 v[86:87], v[86:87], v[132:133], v[88:89] op_sel_hi:[1,0,1]
	v_pk_fma_f32 v[88:89], v[82:83], v[132:133], v[90:91] op_sel_hi:[1,0,1]
	v_pk_fma_f32 v[82:83], v[80:81], v[132:133], v[98:99] op_sel_hi:[1,0,1]
	v_pk_fma_f32 v[84:85], v[84:85], v[132:133], v[96:97] op_sel_hi:[1,0,1]
	s_nop 0
	v_cvt_pk_bf16_f32 v80, v84, v85
	v_cvt_pk_bf16_f32 v81, v86, v87
	v_cvt_pk_bf16_f32 v82, v82, v83
	v_cvt_pk_bf16_f32 v83, v88, v89
	global_store_dwordx4 v[100:101], v[80:83], off offset:256
	v_lshl_add_u64 v[84:85], s[64:65], 0, v[92:93]
	s_waitcnt vmcnt(15)
	v_lshlrev_b32_e32 v86, 16, v184
	v_and_b32_e32 v87, 0xffff0000, v184
	v_lshlrev_b32_e32 v80, 16, v185
	v_and_b32_e32 v81, 0xffff0000, v185
	v_lshlrev_b32_e32 v88, 16, v186
	v_and_b32_e32 v89, 0xffff0000, v186
	v_lshlrev_b32_e32 v82, 16, v187
	v_and_b32_e32 v83, 0xffff0000, v187
	v_pk_mul_f32 v[80:81], v[80:81], s[10:11] op_sel_hi:[1,0]
	v_pk_mul_f32 v[88:89], v[88:89], s[10:11] op_sel_hi:[1,0]
	v_pk_mul_f32 v[82:83], v[82:83], s[10:11] op_sel_hi:[1,0]
	v_pk_mul_f32 v[86:87], v[86:87], s[10:11] op_sel_hi:[1,0]
	v_pk_fma_f32 v[78:79], v[78:79], v[132:133], v[80:81] op_sel_hi:[1,0,1]
	v_pk_fma_f32 v[80:81], v[74:75], v[132:133], v[82:83] op_sel_hi:[1,0,1]
	v_pk_fma_f32 v[74:75], v[72:73], v[132:133], v[88:89] op_sel_hi:[1,0,1]
	v_pk_fma_f32 v[76:77], v[76:77], v[132:133], v[86:87] op_sel_hi:[1,0,1]
	s_nop 0
	v_cvt_pk_bf16_f32 v72, v76, v77
	v_cvt_pk_bf16_f32 v73, v78, v79
	v_cvt_pk_bf16_f32 v74, v74, v75
	v_cvt_pk_bf16_f32 v75, v80, v81
	global_store_dwordx4 v[84:85], v[72:75], off
	v_lshl_add_u64 v[76:77], v[134:135], 0, s[12:13]
	s_waitcnt vmcnt(15)
	v_lshlrev_b32_e32 v80, 16, v188
	v_and_b32_e32 v81, 0xffff0000, v188
	v_lshlrev_b32_e32 v72, 16, v189
	v_and_b32_e32 v73, 0xffff0000, v189
	v_lshlrev_b32_e32 v82, 16, v190
	v_and_b32_e32 v83, 0xffff0000, v190
	v_lshlrev_b32_e32 v74, 16, v191
	v_and_b32_e32 v75, 0xffff0000, v191
	v_pk_mul_f32 v[72:73], v[72:73], s[10:11] op_sel_hi:[1,0]
	v_pk_mul_f32 v[82:83], v[82:83], s[10:11] op_sel_hi:[1,0]
	v_pk_mul_f32 v[74:75], v[74:75], s[10:11] op_sel_hi:[1,0]
	v_pk_mul_f32 v[80:81], v[80:81], s[10:11] op_sel_hi:[1,0]
	v_pk_fma_f32 v[70:71], v[70:71], v[132:133], v[72:73] op_sel_hi:[1,0,1]
	v_pk_fma_f32 v[72:73], v[66:67], v[132:133], v[74:75] op_sel_hi:[1,0,1]
	v_pk_fma_f32 v[66:67], v[64:65], v[132:133], v[82:83] op_sel_hi:[1,0,1]
	v_pk_fma_f32 v[68:69], v[68:69], v[132:133], v[80:81] op_sel_hi:[1,0,1]
	s_nop 0
	v_cvt_pk_bf16_f32 v64, v68, v69
	v_cvt_pk_bf16_f32 v65, v70, v71
	v_cvt_pk_bf16_f32 v66, v66, v67
	v_cvt_pk_bf16_f32 v67, v72, v73
	global_store_dwordx4 v[84:85], v[64:67], off offset:256
	v_lshl_add_u64 v[68:69], s[64:65], 0, v[76:77]
	s_waitcnt vmcnt(15)
	v_lshlrev_b32_e32 v70, 16, v192
	v_and_b32_e32 v71, 0xffff0000, v192
	v_lshlrev_b32_e32 v64, 16, v193
	v_and_b32_e32 v65, 0xffff0000, v193
	v_lshlrev_b32_e32 v72, 16, v194
	v_and_b32_e32 v73, 0xffff0000, v194
	v_lshlrev_b32_e32 v66, 16, v195
	v_and_b32_e32 v67, 0xffff0000, v195
	v_pk_mul_f32 v[64:65], v[64:65], s[10:11] op_sel_hi:[1,0]
	v_pk_mul_f32 v[72:73], v[72:73], s[10:11] op_sel_hi:[1,0]
	v_pk_mul_f32 v[66:67], v[66:67], s[10:11] op_sel_hi:[1,0]
	v_pk_mul_f32 v[70:71], v[70:71], s[10:11] op_sel_hi:[1,0]
	v_pk_fma_f32 v[62:63], v[62:63], v[132:133], v[64:65] op_sel_hi:[1,0,1]
	v_pk_fma_f32 v[64:65], v[58:59], v[132:133], v[66:67] op_sel_hi:[1,0,1]
	v_pk_fma_f32 v[58:59], v[56:57], v[132:133], v[72:73] op_sel_hi:[1,0,1]
	v_pk_fma_f32 v[60:61], v[60:61], v[132:133], v[70:71] op_sel_hi:[1,0,1]
	s_nop 0
	v_cvt_pk_bf16_f32 v56, v60, v61
	v_cvt_pk_bf16_f32 v57, v62, v63
	v_cvt_pk_bf16_f32 v58, v58, v59
	v_cvt_pk_bf16_f32 v59, v64, v65
	global_store_dwordx4 v[68:69], v[56:59], off
	v_lshl_add_u64 v[60:61], v[134:135], 0, s[14:15]
	s_waitcnt vmcnt(15)
	v_lshlrev_b32_e32 v64, 16, v196
	v_and_b32_e32 v65, 0xffff0000, v196
	v_lshlrev_b32_e32 v56, 16, v197
	v_and_b32_e32 v57, 0xffff0000, v197
	v_lshlrev_b32_e32 v66, 16, v198
	v_and_b32_e32 v67, 0xffff0000, v198
	v_lshlrev_b32_e32 v58, 16, v199
	v_and_b32_e32 v59, 0xffff0000, v199
	v_pk_mul_f32 v[56:57], v[56:57], s[10:11] op_sel_hi:[1,0]
	v_pk_mul_f32 v[66:67], v[66:67], s[10:11] op_sel_hi:[1,0]
	v_pk_mul_f32 v[58:59], v[58:59], s[10:11] op_sel_hi:[1,0]
	v_pk_mul_f32 v[64:65], v[64:65], s[10:11] op_sel_hi:[1,0]
	v_pk_fma_f32 v[54:55], v[54:55], v[132:133], v[56:57] op_sel_hi:[1,0,1]
	v_pk_fma_f32 v[56:57], v[50:51], v[132:133], v[58:59] op_sel_hi:[1,0,1]
	v_pk_fma_f32 v[50:51], v[48:49], v[132:133], v[66:67] op_sel_hi:[1,0,1]
	v_pk_fma_f32 v[52:53], v[52:53], v[132:133], v[64:65] op_sel_hi:[1,0,1]
	s_nop 0
	v_cvt_pk_bf16_f32 v48, v52, v53
	v_cvt_pk_bf16_f32 v49, v54, v55
	v_cvt_pk_bf16_f32 v50, v50, v51
	v_cvt_pk_bf16_f32 v51, v56, v57
	global_store_dwordx4 v[68:69], v[48:51], off offset:256
	v_lshl_add_u64 v[52:53], s[64:65], 0, v[60:61]
	s_waitcnt vmcnt(15)
	v_lshlrev_b32_e32 v54, 16, v200
	v_and_b32_e32 v55, 0xffff0000, v200
	v_lshlrev_b32_e32 v48, 16, v201
	v_and_b32_e32 v49, 0xffff0000, v201
	v_lshlrev_b32_e32 v56, 16, v202
	v_and_b32_e32 v57, 0xffff0000, v202
	v_lshlrev_b32_e32 v50, 16, v203
	v_and_b32_e32 v51, 0xffff0000, v203
	v_pk_mul_f32 v[48:49], v[48:49], s[10:11] op_sel_hi:[1,0]
	v_pk_mul_f32 v[56:57], v[56:57], s[10:11] op_sel_hi:[1,0]
	v_pk_mul_f32 v[50:51], v[50:51], s[10:11] op_sel_hi:[1,0]
	v_pk_mul_f32 v[54:55], v[54:55], s[10:11] op_sel_hi:[1,0]
	v_pk_fma_f32 v[46:47], v[46:47], v[132:133], v[48:49] op_sel_hi:[1,0,1]
	v_pk_fma_f32 v[48:49], v[42:43], v[132:133], v[50:51] op_sel_hi:[1,0,1]
	v_pk_fma_f32 v[42:43], v[40:41], v[132:133], v[56:57] op_sel_hi:[1,0,1]
	v_pk_fma_f32 v[44:45], v[44:45], v[132:133], v[54:55] op_sel_hi:[1,0,1]
	s_nop 0
	v_cvt_pk_bf16_f32 v40, v44, v45
	v_cvt_pk_bf16_f32 v41, v46, v47
	v_cvt_pk_bf16_f32 v42, v42, v43
	v_cvt_pk_bf16_f32 v43, v48, v49
	global_store_dwordx4 v[52:53], v[40:43], off
	v_lshl_add_u64 v[44:45], v[134:135], 0, s[16:17]
	s_waitcnt vmcnt(15)
	v_lshlrev_b32_e32 v48, 16, v204
	v_and_b32_e32 v49, 0xffff0000, v204
	v_lshlrev_b32_e32 v40, 16, v205
	v_and_b32_e32 v41, 0xffff0000, v205
	v_lshlrev_b32_e32 v50, 16, v206
	v_and_b32_e32 v51, 0xffff0000, v206
	v_lshlrev_b32_e32 v42, 16, v207
	v_and_b32_e32 v43, 0xffff0000, v207
	v_pk_mul_f32 v[40:41], v[40:41], s[10:11] op_sel_hi:[1,0]
	v_pk_mul_f32 v[50:51], v[50:51], s[10:11] op_sel_hi:[1,0]
	v_pk_mul_f32 v[42:43], v[42:43], s[10:11] op_sel_hi:[1,0]
	v_pk_mul_f32 v[48:49], v[48:49], s[10:11] op_sel_hi:[1,0]
	v_pk_fma_f32 v[38:39], v[38:39], v[132:133], v[40:41] op_sel_hi:[1,0,1]
	v_pk_fma_f32 v[40:41], v[34:35], v[132:133], v[42:43] op_sel_hi:[1,0,1]
	v_pk_fma_f32 v[34:35], v[32:33], v[132:133], v[50:51] op_sel_hi:[1,0,1]
	v_pk_fma_f32 v[36:37], v[36:37], v[132:133], v[48:49] op_sel_hi:[1,0,1]
	s_nop 0
	v_cvt_pk_bf16_f32 v32, v36, v37
	v_cvt_pk_bf16_f32 v33, v38, v39
	v_cvt_pk_bf16_f32 v34, v34, v35
	v_cvt_pk_bf16_f32 v35, v40, v41
	global_store_dwordx4 v[52:53], v[32:35], off offset:256
	v_lshl_add_u64 v[36:37], s[64:65], 0, v[44:45]
	s_waitcnt vmcnt(15)
	v_lshlrev_b32_e32 v38, 16, v208
	v_and_b32_e32 v39, 0xffff0000, v208
	v_lshlrev_b32_e32 v32, 16, v209
	v_and_b32_e32 v33, 0xffff0000, v209
	v_lshlrev_b32_e32 v40, 16, v210
	v_and_b32_e32 v41, 0xffff0000, v210
	v_lshlrev_b32_e32 v34, 16, v211
	v_and_b32_e32 v35, 0xffff0000, v211
	v_pk_mul_f32 v[32:33], v[32:33], s[10:11] op_sel_hi:[1,0]
	v_pk_mul_f32 v[40:41], v[40:41], s[10:11] op_sel_hi:[1,0]
	v_pk_mul_f32 v[34:35], v[34:35], s[10:11] op_sel_hi:[1,0]
	v_pk_mul_f32 v[38:39], v[38:39], s[10:11] op_sel_hi:[1,0]
	v_pk_fma_f32 v[30:31], v[30:31], v[132:133], v[32:33] op_sel_hi:[1,0,1]
	v_pk_fma_f32 v[32:33], v[26:27], v[132:133], v[34:35] op_sel_hi:[1,0,1]
	v_pk_fma_f32 v[26:27], v[24:25], v[132:133], v[40:41] op_sel_hi:[1,0,1]
	v_pk_fma_f32 v[28:29], v[28:29], v[132:133], v[38:39] op_sel_hi:[1,0,1]
	s_nop 0
	v_cvt_pk_bf16_f32 v24, v28, v29
	v_cvt_pk_bf16_f32 v25, v30, v31
	v_cvt_pk_bf16_f32 v26, v26, v27
	v_cvt_pk_bf16_f32 v27, v32, v33
	global_store_dwordx4 v[36:37], v[24:27], off
	v_lshl_add_u64 v[28:29], v[134:135], 0, s[18:19]
	s_waitcnt vmcnt(15)
	v_lshlrev_b32_e32 v32, 16, v212
	v_and_b32_e32 v33, 0xffff0000, v212
	v_lshlrev_b32_e32 v24, 16, v213
	v_and_b32_e32 v25, 0xffff0000, v213
	v_lshlrev_b32_e32 v34, 16, v214
	v_and_b32_e32 v35, 0xffff0000, v214
	v_lshlrev_b32_e32 v26, 16, v215
	v_and_b32_e32 v27, 0xffff0000, v215
	v_pk_mul_f32 v[24:25], v[24:25], s[10:11] op_sel_hi:[1,0]
	v_pk_mul_f32 v[34:35], v[34:35], s[10:11] op_sel_hi:[1,0]
	v_pk_mul_f32 v[26:27], v[26:27], s[10:11] op_sel_hi:[1,0]
	v_pk_mul_f32 v[32:33], v[32:33], s[10:11] op_sel_hi:[1,0]
	v_pk_fma_f32 v[22:23], v[22:23], v[132:133], v[24:25] op_sel_hi:[1,0,1]
	v_pk_fma_f32 v[24:25], v[18:19], v[132:133], v[26:27] op_sel_hi:[1,0,1]
	v_pk_fma_f32 v[18:19], v[16:17], v[132:133], v[34:35] op_sel_hi:[1,0,1]
	v_pk_fma_f32 v[20:21], v[20:21], v[132:133], v[32:33] op_sel_hi:[1,0,1]
	s_nop 0
	v_cvt_pk_bf16_f32 v16, v20, v21
	v_cvt_pk_bf16_f32 v17, v22, v23
	v_cvt_pk_bf16_f32 v18, v18, v19
	v_cvt_pk_bf16_f32 v19, v24, v25
	global_store_dwordx4 v[36:37], v[16:19], off offset:256
	v_lshl_add_u64 v[20:21], s[64:65], 0, v[28:29]
	s_waitcnt vmcnt(15)
	v_lshlrev_b32_e32 v22, 16, v216
	v_and_b32_e32 v23, 0xffff0000, v216
	v_lshlrev_b32_e32 v16, 16, v217
	v_and_b32_e32 v17, 0xffff0000, v217
	v_lshlrev_b32_e32 v24, 16, v218
	v_and_b32_e32 v25, 0xffff0000, v218
	v_lshlrev_b32_e32 v18, 16, v219
	v_and_b32_e32 v19, 0xffff0000, v219
	v_pk_mul_f32 v[16:17], v[16:17], s[10:11] op_sel_hi:[1,0]
	v_pk_mul_f32 v[24:25], v[24:25], s[10:11] op_sel_hi:[1,0]
	v_pk_mul_f32 v[18:19], v[18:19], s[10:11] op_sel_hi:[1,0]
	v_pk_mul_f32 v[22:23], v[22:23], s[10:11] op_sel_hi:[1,0]
	v_pk_fma_f32 v[14:15], v[14:15], v[132:133], v[16:17] op_sel_hi:[1,0,1]
	v_pk_fma_f32 v[16:17], v[10:11], v[132:133], v[18:19] op_sel_hi:[1,0,1]
	v_pk_fma_f32 v[10:11], v[8:9], v[132:133], v[24:25] op_sel_hi:[1,0,1]
	v_pk_fma_f32 v[12:13], v[12:13], v[132:133], v[22:23] op_sel_hi:[1,0,1]
	s_nop 0
	v_cvt_pk_bf16_f32 v8, v12, v13
	v_cvt_pk_bf16_f32 v9, v14, v15
	v_cvt_pk_bf16_f32 v10, v10, v11
	v_cvt_pk_bf16_f32 v11, v16, v17
	global_store_dwordx4 v[20:21], v[8:11], off
	s_waitcnt vmcnt(15)
	v_lshlrev_b32_e32 v12, 16, v220
	v_and_b32_e32 v13, 0xffff0000, v220
	v_lshlrev_b32_e32 v8, 16, v221
	v_and_b32_e32 v9, 0xffff0000, v221
	v_lshlrev_b32_e32 v14, 16, v222
	v_and_b32_e32 v15, 0xffff0000, v222
	v_lshlrev_b32_e32 v10, 16, v223
	v_and_b32_e32 v11, 0xffff0000, v223
	v_pk_mul_f32 v[8:9], v[8:9], s[10:11] op_sel_hi:[1,0]
	v_pk_mul_f32 v[14:15], v[14:15], s[10:11] op_sel_hi:[1,0]
	v_pk_mul_f32 v[10:11], v[10:11], s[10:11] op_sel_hi:[1,0]
	v_pk_mul_f32 v[12:13], v[12:13], s[10:11] op_sel_hi:[1,0]
	v_pk_fma_f32 v[6:7], v[6:7], v[132:133], v[8:9] op_sel_hi:[1,0,1]
	v_pk_fma_f32 v[8:9], v[2:3], v[132:133], v[10:11] op_sel_hi:[1,0,1]
	v_pk_fma_f32 v[2:3], v[0:1], v[132:133], v[14:15] op_sel_hi:[1,0,1]
	v_pk_fma_f32 v[4:5], v[4:5], v[132:133], v[12:13] op_sel_hi:[1,0,1]
	s_nop 0
	v_cvt_pk_bf16_f32 v0, v4, v5
	v_cvt_pk_bf16_f32 v1, v6, v7
	v_cvt_pk_bf16_f32 v2, v2, v3
	v_cvt_pk_bf16_f32 v3, v8, v9
	global_store_dwordx4 v[20:21], v[0:3], off offset:256
	s_cbranch_vccnz .LBB0_1614
	s_andn2_b64 vcc, exec, s[4:5]
	s_cbranch_vccnz .LBB0_1613
	s_barrier
	s_branch .LBB0_1613

	.amdhsa_kernel _Z10fwd_kernel4Args
		.amdhsa_group_segment_fixed_size 0
		.amdhsa_private_segment_fixed_size 0
		.amdhsa_kernarg_size 416
		.amdhsa_user_sgpr_count 2
		.amdhsa_user_sgpr_dispatch_ptr 0
		.amdhsa_user_sgpr_queue_ptr 0
		.amdhsa_user_sgpr_kernarg_segment_ptr 1
		.amdhsa_user_sgpr_dispatch_id 0
		.amdhsa_user_sgpr_kernarg_preload_length 0
		.amdhsa_user_sgpr_kernarg_preload_offset 0
		.amdhsa_user_sgpr_private_segment_size 0
		.amdhsa_uses_dynamic_stack 0
		.amdhsa_enable_private_segment 0
		.amdhsa_system_sgpr_workgroup_id_x 1
		.amdhsa_system_sgpr_workgroup_id_y 0
		.amdhsa_system_sgpr_workgroup_id_z 0
		.amdhsa_system_sgpr_workgroup_info 0
		.amdhsa_system_vgpr_workitem_id 0
		.amdhsa_next_free_vgpr 256
		.amdhsa_next_free_sgpr 102
		.amdhsa_accum_offset 256
		.amdhsa_reserve_vcc 1
		.amdhsa_float_round_mode_32 0
		.amdhsa_float_round_mode_16_64 0
		.amdhsa_float_denorm_mode_32 3
		.amdhsa_float_denorm_mode_16_64 3
		.amdhsa_dx10_clamp 1
		.amdhsa_ieee_mode 1
		.amdhsa_fp16_overflow 0
		.amdhsa_tg_split 0
		.amdhsa_exception_fp_ieee_invalid_op 0
		.amdhsa_exception_fp_denorm_src 0
		.amdhsa_exception_fp_ieee_div_zero 0
		.amdhsa_exception_fp_ieee_overflow 0
		.amdhsa_exception_fp_ieee_underflow 0
		.amdhsa_exception_fp_ieee_inexact 0
		.amdhsa_exception_int_div_zero 0
	.end_amdhsa_kernel

amdhsa.kernels:
  - .agpr_count:     0
    .args:
      - .offset:         0
        .size:           160
        .value_kind:     by_value
      - .offset:         160
        .size:           4
        .value_kind:     hidden_block_count_x
      - .offset:         164
        .size:           4
        .value_kind:     hidden_block_count_y
      - .offset:         168
        .size:           4
        .value_kind:     hidden_block_count_z
      - .offset:         172
        .size:           2
        .value_kind:     hidden_group_size_x
      - .offset:         174
        .size:           2
        .value_kind:     hidden_group_size_y
      - .offset:         176
        .size:           2
        .value_kind:     hidden_group_size_z
      - .offset:         178
        .size:           2
        .value_kind:     hidden_remainder_x
      - .offset:         180
        .size:           2
        .value_kind:     hidden_remainder_y
      - .offset:         182
        .size:           2
        .value_kind:     hidden_remainder_z
      - .offset:         200
        .size:           8
        .value_kind:     hidden_global_offset_x
      - .offset:         208
        .size:           8
        .value_kind:     hidden_global_offset_y
      - .offset:         216
        .size:           8
        .value_kind:     hidden_global_offset_z
      - .offset:         224
        .size:           2
        .value_kind:     hidden_grid_dims
      - .offset:         280
        .size:           4
        .value_kind:     hidden_dynamic_lds_size
    .group_segment_fixed_size: 0
    .kernarg_segment_align: 8
    .kernarg_segment_size: 416
    .language:       OpenCL C
    .language_version:
      - 2
      - 0
    .max_flat_workgroup_size: 512
    .name:           _Z10fwd_kernel4Args
    .private_segment_fixed_size: 0
    .sgpr_count:     108
    .sgpr_spill_count: 68
    .symbol:         _Z10fwd_kernel4Args.kd
    .uniform_work_group_size: 1
    .uses_dynamic_stack: false
    .vgpr_count:     256
    .vgpr_spill_count: 0
    .wavefront_size: 64
